# N1: next-row prefetch kept in flight + gate loads overlapped with expert-row loads; FIN gate1 wait removed; topk per-wave counts read with 2 LDS ops
# speedup vs baseline: 1.0246x; 1.0125x over previous
.LBB0_226:
	s_add_i32 s12, s10, s80
	s_cmp_gt_i32 s12, 0x81ff
	s_cselect_b64 s[14:15], -1, 0
	s_and_b64 vcc, exec, s[14:15]
	s_cbranch_vccnz .LBB0_243
	s_and_b64 vcc, exec, s[8:9]
	s_cbranch_vccz .LBB0_231
	s_ashr_i32 s13, s12, 31
	s_lshl_b64 s[16:17], s[12:13], 11
	v_lshl_or_b32 v24, s12, 4, v128
	v_lshl_add_u64 v[16:17], v[116:117], 0, s[16:17]
	v_ashrrev_i32_e32 v25, 31, v24
	global_load_dwordx2 v[100:101], v[16:17], off
	global_load_dwordx2 v[104:105], v[16:17], off offset:512
	global_load_dwordx2 v[108:109], v[16:17], off offset:1024
	global_load_dwordx2 v[112:113], v[16:17], off offset:1536
	v_lshl_add_u64 v[24:25], v[24:25], 2, s[6:7]
	global_load_dword v136, v[24:25], off
	s_cbranch_execnz .LBB0_232

.LBB0_235:
	s_lshl_b64 s[16:17], s[16:17], 10
	v_lshl_add_u64 v[36:37], v[118:119], 0, s[16:17]
	s_lshl_b64 s[16:17], s[18:19], 10
	v_lshl_add_u64 v[38:39], v[118:119], 0, s[16:17]
	global_load_dword v33, v[36:37], off nt
	global_load_dword v35, v[38:39], off nt
	global_load_dword v46, v[36:37], off offset:256 nt
	global_load_dword v137, v[38:39], off offset:256 nt
	global_load_dword v144, v[36:37], off offset:512 nt
	global_load_dword v148, v[38:39], off offset:512 nt
	global_load_dword v152, v[36:37], off offset:768 nt
	global_load_dword v156, v[38:39], off offset:768 nt
	s_and_b32 s11, s13, s11
	s_cmp_lg_u32 s11, 0
	s_waitcnt vmcnt(7)
	v_mul_f32_e32 v34, 0x3d800000, v34
	v_mul_f32_e32 v32, 0x3d800000, v32
	v_cvt_pk_f32_fp8_e32 v[36:37], v33
	s_waitcnt vmcnt(6)
	v_cvt_pk_f32_fp8_e32 v[40:41], v35
	v_cvt_pk_f32_fp8_sdwa v[42:43], v35 src0_sel:WORD_1
	s_waitcnt vmcnt(4)
	v_cvt_pk_f32_fp8_e32 v[138:139], v137
	v_cvt_pk_f32_fp8_sdwa v[140:141], v137 src0_sel:WORD_1
	s_waitcnt vmcnt(2)
	v_cvt_pk_f32_fp8_e32 v[146:147], v148
	s_waitcnt vmcnt(1)
	v_cvt_pk_f32_fp8_e32 v[150:151], v152
	v_cvt_pk_f32_fp8_sdwa v[152:153], v152 src0_sel:WORD_1
	s_waitcnt vmcnt(0)
	v_cvt_pk_f32_fp8_e32 v[154:155], v156
	v_cvt_pk_f32_fp8_sdwa v[156:157], v156 src0_sel:WORD_1
	v_cvt_pk_f32_fp8_sdwa v[148:149], v148 src0_sel:WORD_1
	v_cvt_pk_f32_fp8_sdwa v[38:39], v33 src0_sel:WORD_1
	v_cvt_pk_f32_fp8_e32 v[44:45], v46
	v_cvt_pk_f32_fp8_sdwa v[46:47], v46 src0_sel:WORD_1
	v_cvt_pk_f32_fp8_e32 v[142:143], v144
	v_cvt_pk_f32_fp8_sdwa v[144:145], v144 src0_sel:WORD_1
	v_mul_f32_e32 v158, v32, v156
	v_mov_b32_e32 v35, v32
	v_mov_b32_e32 v156, v153
	v_pk_mul_f32 v[40:41], v[32:33], v[40:41] op_sel_hi:[0,1]
	v_pk_mul_f32 v[42:43], v[32:33], v[42:43] op_sel_hi:[0,1]
	v_pk_mul_f32 v[138:139], v[32:33], v[138:139] op_sel_hi:[0,1]
	v_pk_mul_f32 v[140:141], v[32:33], v[140:141] op_sel_hi:[0,1]
	v_pk_mul_f32 v[146:147], v[32:33], v[146:147] op_sel_hi:[0,1]
	v_pk_mul_f32 v[148:149], v[32:33], v[148:149] op_sel_hi:[0,1]
	v_pk_mul_f32 v[154:155], v[32:33], v[154:155] op_sel_hi:[0,1]
	v_pk_mul_f32 v[32:33], v[34:35], v[156:157]
	v_mul_f32_e32 v152, v34, v152
	v_mov_b32_e32 v153, v32
	v_mov_b32_e32 v159, v33
	v_pk_fma_f32 v[32:33], v[34:35], v[36:37], v[40:41] op_sel_hi:[0,1,1]
	v_pk_fma_f32 v[36:37], v[34:35], v[38:39], v[42:43] op_sel_hi:[0,1,1]
	v_pk_fma_f32 v[38:39], v[34:35], v[44:45], v[138:139] op_sel_hi:[0,1,1]
	v_pk_fma_f32 v[40:41], v[34:35], v[46:47], v[140:141] op_sel_hi:[0,1,1]
	v_pk_fma_f32 v[42:43], v[34:35], v[142:143], v[146:147] op_sel_hi:[0,1,1]
	v_pk_fma_f32 v[44:45], v[34:35], v[144:145], v[148:149] op_sel_hi:[0,1,1]
	v_pk_fma_f32 v[34:35], v[34:35], v[150:151], v[154:155] op_sel_hi:[0,1,1]
	v_pk_add_f32 v[46:47], v[152:153], v[158:159]
	v_pk_add_f32 v[28:29], v[28:29], v[34:35]
	v_pk_add_f32 v[30:31], v[30:31], v[46:47]
	v_pk_add_f32 v[26:27], v[26:27], v[44:45]
	v_pk_add_f32 v[24:25], v[24:25], v[42:43]
	v_pk_add_f32 v[22:23], v[22:23], v[40:41]
	v_pk_add_f32 v[20:21], v[20:21], v[38:39]
	v_pk_add_f32 v[18:19], v[18:19], v[36:37]
	v_pk_add_f32 v[16:17], v[16:17], v[32:33]
	s_cbranch_scc0 .LBB0_239
.LBB0_236:
	s_add_i32 s16, s11, -1
	s_ff1_i32_b32 s13, s11
	s_and_b32 s11, s16, s11
	v_sub_co_u32_e64 v32, s[16:17], s11, 1
	s_ff1_i32_b32 s18, s11
	s_and_b64 vcc, s[16:17], exec
	v_readlane_b32 s16, v135, s13
	s_cselect_b32 s20, s13, s18
	s_ashr_i32 s17, s16, 31
	s_lshl_b64 s[18:19], s[16:17], 2
	s_add_u32 s18, s24, s18
	s_addc_u32 s19, s25, s19
	global_load_dword v34, v65, s[18:19]
	v_readlane_b32 s18, v135, s20
	v_readfirstlane_b32 s13, v32
	s_ashr_i32 s19, s18, 31
	v_mov_b32_e32 v32, 0
	s_cbranch_vccnz .LBB0_235
	s_lshl_b64 s[20:21], s[18:19], 2
	s_add_u32 s20, s24, s20
	s_addc_u32 s21, s25, s21
	global_load_dword v32, v65, s[20:21]
	s_branch .LBB0_235

.LBB0_239:
	s_ashr_i32 s11, s10, 31
	s_lshl_b64 s[16:17], s[10:11], 11
	v_lshl_add_u64 v[32:33], v[116:117], 0, s[16:17]
	s_waitcnt lgkmcnt(0)
	v_pk_fma_f32 v[18:19], v[68:69], v[18:19], v[2:3]
	v_pk_fma_f32 v[16:17], v[66:67], v[16:17], v[0:1]
	v_pk_fma_f32 v[22:23], v[58:59], v[22:23], v[6:7]
	v_cvt_pk_bf16_f32 v34, v16, v17
	v_cvt_pk_bf16_f32 v35, v18, v19
	global_store_dwordx2 v[32:33], v[34:35], off
	v_pk_fma_f32 v[20:21], v[56:57], v[20:21], v[4:5]
	v_pk_fma_f32 v[26:27], v[54:55], v[26:27], v[10:11]
	v_cvt_pk_bf16_f32 v34, v20, v21
	v_cvt_pk_bf16_f32 v35, v22, v23
	global_store_dwordx2 v[32:33], v[34:35], off offset:512
	v_pk_fma_f32 v[24:25], v[52:53], v[24:25], v[8:9]
	s_waitcnt vmcnt(2)
	v_pk_fma_f32 v[30:31], v[50:51], v[30:31], v[14:15]
	v_cvt_pk_bf16_f32 v34, v24, v25
	v_cvt_pk_bf16_f32 v35, v26, v27
	global_store_dwordx2 v[32:33], v[34:35], off offset:1024
	v_pk_fma_f32 v[28:29], v[48:49], v[28:29], v[12:13]
	s_nop 0
	v_cvt_pk_bf16_f32 v34, v28, v29
	v_cvt_pk_bf16_f32 v35, v30, v31
	global_store_dwordx2 v[32:33], v[34:35], off offset:1536
	v_lshlrev_b32_e32 v98, 16, v100
	v_and_b32_e32 v99, 0xffff0000, v100
	v_lshlrev_b32_e32 v100, 16, v101
	v_and_b32_e32 v101, 0xffff0000, v101
	v_lshlrev_b32_e32 v102, 16, v104
	v_and_b32_e32 v103, 0xffff0000, v104
	v_lshlrev_b32_e32 v104, 16, v105
	v_and_b32_e32 v105, 0xffff0000, v105
	v_lshlrev_b32_e32 v106, 16, v108
	v_and_b32_e32 v107, 0xffff0000, v108
	v_lshlrev_b32_e32 v108, 16, v109
	v_and_b32_e32 v109, 0xffff0000, v109
	v_lshlrev_b32_e32 v110, 16, v112
	v_and_b32_e32 v111, 0xffff0000, v112
	v_lshlrev_b32_e32 v112, 16, v113
	v_and_b32_e32 v113, 0xffff0000, v113
	v_mov_b64_e32 v[46:47], v[30:31]
	v_mov_b64_e32 v[44:45], v[28:29]
	v_mov_b64_e32 v[42:43], v[26:27]
	v_mov_b64_e32 v[40:41], v[24:25]
	v_mov_b64_e32 v[38:39], v[22:23]
	v_mov_b64_e32 v[36:37], v[20:21]
	v_mov_b64_e32 v[34:35], v[18:19]
	v_mov_b64_e32 v[32:33], v[16:17]
	s_branch .LBB0_221

.LBB0_1117:
	s_or_b64 exec, exec, s[66:67]
	s_waitcnt lgkmcnt(0)
	s_barrier
	v_mov_b32_e32 v90, s74
	ds_read2_b64 v[106:109], v90 offset1:1
	ds_read2_b64 v[110:113], v90 offset0:2 offset1:3
	s_add_i32 s70, s70, -1
	s_add_i32 s71, s71, -8
	s_cmp_eq_u32 s70, -1
	s_waitcnt lgkmcnt(0)
	v_add_u32_e32 v106, v106, v107
	v_add_u32_e32 v108, v108, v109
	v_add_u32_e32 v110, v110, v111
	v_add_u32_e32 v112, v112, v113
	v_add_u32_e32 v106, v106, v108
	v_add_u32_e32 v110, v110, v112
	v_add_u32_e32 v90, v106, v110
	v_cmp_gt_u32_e64 s[0:1], s82, v90
	s_nop 1
	v_cndmask_b32_e64 v64, v88, v64, s[0:1]
	s_cbranch_scc1 .LBB0_1120

.LBB0_1576:
	s_lshl_b64 s[10:11], s[10:11], 10
	v_lshl_add_u64 v[102:103], v[52:53], 0, s[10:11]
	s_lshl_b64 s[10:11], s[12:13], 10
	v_lshl_add_u64 v[104:105], v[52:53], 0, s[10:11]
	global_load_dword v106, v[102:103], off nt
	global_load_dword v110, v[104:105], off nt
	global_load_dword v114, v[102:103], off offset:256 nt
	global_load_dword v118, v[104:105], off offset:256 nt
	global_load_dword v122, v[102:103], off offset:512 nt
	global_load_dword v126, v[104:105], off offset:512 nt
	global_load_dword v134, v[104:105], off offset:768 nt
	global_load_dword v130, v[102:103], off offset:768 nt
	s_waitcnt vmcnt(8)
	v_mul_f32_e32 v90, 0x3d800000, v90
	v_mul_f32_e32 v102, 0x3d800000, v101
	v_mov_b32_e32 v103, v90
	s_and_b32 s10, s21, s20
	s_cmp_eq_u32 s10, 0
	s_waitcnt vmcnt(6)
	v_cvt_pk_f32_fp8_e32 v[108:109], v110
	v_cvt_pk_f32_fp8_sdwa v[110:111], v110 src0_sel:WORD_1
	s_waitcnt vmcnt(4)
	v_cvt_pk_f32_fp8_e32 v[116:117], v118
	v_cvt_pk_f32_fp8_sdwa v[118:119], v118 src0_sel:WORD_1
	s_waitcnt vmcnt(2)
	v_cvt_pk_f32_fp8_e32 v[124:125], v126
	s_waitcnt vmcnt(1)
	v_cvt_pk_f32_fp8_e32 v[132:133], v134
	s_waitcnt vmcnt(0)
	v_cvt_pk_f32_fp8_e32 v[128:129], v130
	v_cvt_pk_f32_fp8_sdwa v[130:131], v130 src0_sel:WORD_1
	v_cvt_pk_f32_fp8_sdwa v[134:135], v134 src0_sel:WORD_1
	v_cvt_pk_f32_fp8_sdwa v[126:127], v126 src0_sel:WORD_1
	v_cvt_pk_f32_fp8_e32 v[104:105], v106
	v_cvt_pk_f32_fp8_sdwa v[106:107], v106 src0_sel:WORD_1
	v_cvt_pk_f32_fp8_e32 v[112:113], v114
	v_cvt_pk_f32_fp8_sdwa v[114:115], v114 src0_sel:WORD_1
	v_cvt_pk_f32_fp8_e32 v[120:121], v122
	v_cvt_pk_f32_fp8_sdwa v[122:123], v122 src0_sel:WORD_1
	v_mul_f32_e32 v136, v90, v134
	v_mov_b32_e32 v134, v131
	v_pk_mul_f32 v[108:109], v[90:91], v[108:109] op_sel_hi:[0,1]
	v_pk_mul_f32 v[110:111], v[90:91], v[110:111] op_sel_hi:[0,1]
	v_pk_mul_f32 v[116:117], v[90:91], v[116:117] op_sel_hi:[0,1]
	v_pk_mul_f32 v[118:119], v[90:91], v[118:119] op_sel_hi:[0,1]
	v_pk_mul_f32 v[124:125], v[90:91], v[124:125] op_sel_hi:[0,1]
	v_pk_mul_f32 v[126:127], v[90:91], v[126:127] op_sel_hi:[0,1]
	v_pk_mul_f32 v[132:133], v[90:91], v[132:133] op_sel_hi:[0,1]
	v_pk_mul_f32 v[134:135], v[102:103], v[134:135]
	v_mul_f32_e32 v130, v102, v130
	v_pk_fma_f32 v[104:105], v[102:103], v[104:105], v[108:109] op_sel_hi:[0,1,1]
	v_pk_fma_f32 v[106:107], v[102:103], v[106:107], v[110:111] op_sel_hi:[0,1,1]
	v_pk_fma_f32 v[108:109], v[102:103], v[112:113], v[116:117] op_sel_hi:[0,1,1]
	v_pk_fma_f32 v[110:111], v[102:103], v[114:115], v[118:119] op_sel_hi:[0,1,1]
	v_pk_fma_f32 v[112:113], v[102:103], v[120:121], v[124:125] op_sel_hi:[0,1,1]
	v_pk_fma_f32 v[114:115], v[102:103], v[122:123], v[126:127] op_sel_hi:[0,1,1]
	v_pk_fma_f32 v[102:103], v[102:103], v[128:129], v[132:133] op_sel_hi:[0,1,1]
	v_mov_b32_e32 v131, v134
	v_mov_b32_e32 v137, v135
	v_pk_add_f32 v[74:75], v[74:75], v[102:103]
	v_pk_add_f32 v[102:103], v[130:131], v[136:137]
	v_pk_add_f32 v[80:81], v[80:81], v[114:115]
	v_pk_add_f32 v[78:79], v[78:79], v[112:113]
	v_pk_add_f32 v[84:85], v[84:85], v[110:111]
	v_pk_add_f32 v[82:83], v[82:83], v[108:109]
	v_pk_add_f32 v[88:89], v[88:89], v[106:107]
	v_pk_add_f32 v[76:77], v[76:77], v[102:103]
	v_pk_add_f32 v[86:87], v[86:87], v[104:105]
	s_cbranch_scc1 .LBB0_1569
.LBB0_1577:
	s_add_i32 s11, s10, -1
	s_and_b32 s20, s11, s10
	s_ff1_i32_b32 s12, s10
	v_sub_co_u32_e64 v90, s[10:11], s20, 1
	s_ff1_i32_b32 s13, s20
	s_and_b64 vcc, s[10:11], exec
	v_readlane_b32 s10, v99, s12
	s_cselect_b32 s22, s12, s13
	s_ashr_i32 s11, s10, 31
	s_lshl_b64 s[12:13], s[10:11], 2
	s_add_u32 s12, s15, s12
	s_addc_u32 s13, s16, s13
	global_load_dword v101, v49, s[12:13]
	v_readlane_b32 s12, v99, s22
	v_readfirstlane_b32 s21, v90
	s_ashr_i32 s13, s12, 31
	v_mov_b32_e32 v90, 0
	s_cbranch_vccnz .LBB0_1576
	s_lshl_b64 s[22:23], s[12:13], 2
	s_add_u32 s22, s15, s22
	s_addc_u32 s23, s16, s23
	global_load_dword v90, v49, s[22:23]
	s_branch .LBB0_1576
